# peersel last stage: PEER_CAND row loaded once per phase, the 14 conditional candidate blocks (one LDS round trip each) batched into 28 reads + one wait
# speedup vs baseline: 1.0049x; 1.0002x over previous
; DI int tidx() { int t = threadIdx.x & 255; asm volatile("" : "+v"(t)); return t; }
; DI void peer_select_unit(const Params& p, int unit, char* lds, const bf16x8 (&kb)[4][4]) {
;     ...
;     const int set = wid >> 1, kh = wid & 1;
;     bf16x8 qa[2][4];
; #pragma unroll
;     for (int mt = 0; mt < 2; ++mt)
; #pragma unroll
;       for (int kk = 0; kk < 4; ++kk) qa[mt][kk] = *(const bf16x8*)(qy + (size_t)(t0 + 16 * mt + fr) * 2048 + h * 256 + set * 128 + kk * 32 + fq * 8);
; DI void phase_peersel(const Params& p, int bid, int nb, char* lds) {
;   const int lane = tidx() & 63, wid = tidx() >> 6, fr = lane & 15, fq = lane >> 4;
;   const bf16_t* keys = (const bf16_t*)(p.ws + WS_KEYS) + (wid >> 1) * 16384 + (wid & 1) * 64 * 128;
;   bf16x8 kb[4][4];
; #pragma unroll
;   for (int nj = 0; nj < 4; ++nj)
; #pragma unroll
;     for (int kk = 0; kk < 4; ++kk) kb[nj][kk] = *(const bf16x8*)(keys + (16 * nj + fr) * 128 + kk * 32 + fq * 8);
;   for (int u = bid; u < 8192; u += nb) peer_select_unit(p, u, lds, kb);
.LBB0_1648:
	s_or_b64 exec, exec, s[0:1]
	v_and_b32_e32 v248, 3, v206
	v_lshlrev_b32_e32 v248, 4, v248
	s_getpc_b64 s[0:1]
	s_add_u32 s0, s0, _ZL9PEER_CAND@rel32@lo+4
	s_addc_u32 s1, s1, _ZL9PEER_CAND@rel32@hi+12
	global_load_dwordx4 v[244:247], v248, s[0:1]
	s_waitcnt vmcnt(0)
	s_movk_i32 s0, 0x2000
	s_waitcnt lgkmcnt(0)
	v_mov_b32_e32 v0, v206
	v_mov_b32_e32 v1, v206
	v_cmp_gt_i32_e32 vcc, s0, v176
	s_barrier
	s_and_saveexec_b64 s[52:53], vcc
	s_cbranch_execz .LBB0_1683
	v_lshlrev_b32_e32 v2, 7, v1
	v_and_b32_e32 v2, 0xffffc000, v2
	v_readlane_b32 s2, v250, 7
	v_ashrrev_i32_e32 v3, 31, v2
	v_readlane_b32 s3, v250, 8
	v_lshlrev_b32_e32 v1, 8, v1
	v_and_b32_e32 v64, 0x4000, v1
	v_lshl_add_u64 v[2:3], v[2:3], 1, s[2:3]
	v_mov_b32_e32 v65, 0
	v_lshl_add_u64 v[2:3], v[2:3], 0, v[64:65]
	v_and_b32_e32 v64, 48, v0
	v_lshlrev_b32_e32 v0, 8, v0
	v_lshl_add_u64 v[2:3], v[2:3], 0, v[64:65]
	v_and_b32_e32 v64, 0xf00, v0
	v_lshl_add_u64 v[40:41], v[2:3], 0, v[64:65]
	s_movk_i32 s1, 0x1000
	v_add_co_u32_e32 v66, vcc, s1, v40
	global_load_dwordx4 v[0:3], v[40:41], off
	global_load_dwordx4 v[4:7], v[40:41], off offset:64
	global_load_dwordx4 v[8:11], v[40:41], off offset:128
	global_load_dwordx4 v[12:15], v[40:41], off offset:192
	v_addc_co_u32_e32 v67, vcc, 0, v41, vcc
	v_add_co_u32_e32 v68, vcc, s0, v40
	s_movk_i32 s0, 0x3000
	s_nop 0
	v_addc_co_u32_e32 v69, vcc, 0, v41, vcc
	v_add_co_u32_e32 v70, vcc, s0, v40
	global_load_dwordx4 v[16:19], v[66:67], off offset:64
	global_load_dwordx4 v[20:23], v[66:67], off offset:128
	global_load_dwordx4 v[24:27], v[68:69], off
	global_load_dwordx4 v[28:31], v[68:69], off offset:64
	global_load_dwordx4 v[32:35], v[68:69], off offset:128
	global_load_dwordx4 v[36:39], v[68:69], off offset:192
	v_addc_co_u32_e32 v71, vcc, 0, v41, vcc
	global_load_dwordx4 v[40:43], v[66:67], off offset:192
	global_load_dwordx4 v[44:47], v[70:71], off
	global_load_dwordx4 v[48:51], v[70:71], off offset:64
	global_load_dwordx4 v[52:55], v[70:71], off offset:128
	global_load_dwordx4 v[56:59], v[68:69], off offset:-4096
	global_load_dwordx4 v[60:63], v[70:71], off offset:192
	s_add_u32 s60, s84, 0x12000000
	s_addc_u32 s61, s85, 0
	s_add_u32 s62, s84, 0x13000000
	s_addc_u32 s63, s85, 0
	s_mov_b64 s[64:65], 0
	s_movk_i32 s2, 0x210
	s_movk_i32 s3, 0x7f
	s_movk_i32 s18, 0x80
	s_movk_i32 s19, 0xff
	s_movk_i32 s68, 0x1fff
	v_mov_b32_e32 v72, v176
	v_and_b32_e32 v182, 15, v206
	v_lshlrev_b32_e32 v182, 12, v182
	v_bfe_u32 v183, v206, 4, 2
	v_lshl_or_b32 v182, v183, 4, v182
	v_lshrrev_b32_e32 v183, 7, v206
	v_lshl_or_b32 v182, v183, 8, v182
	v_mov_b32_e32 v183, 0
	v_lshl_add_u64 v[182:183], s[58:59], 0, v[182:183]
	v_mov_b32_e32 v184, v72
	v_lshrrev_b32_e32 v185, 3, v184
	v_lshlrev_b32_e32 v185, 17, v185
	v_and_b32_e32 v184, 7, v184
	v_lshl_or_b32 v184, v184, 9, v185
	v_mov_b32_e32 v185, 0
	v_lshl_add_u64 v[184:185], v[182:183], 0, v[184:185]
	v_mov_b32_e32 v186, 0x10000
	v_mov_b32_e32 v187, 0
	v_lshl_add_u64 v[186:187], v[184:185], 0, v[186:187]
	global_load_dwordx4 v[148:151], v[184:185], off
	global_load_dwordx4 v[152:155], v[184:185], off offset:64
	global_load_dwordx4 v[156:159], v[186:187], off
	global_load_dwordx4 v[160:163], v[186:187], off offset:64
	global_load_dwordx4 v[164:167], v[184:185], off offset:128
	global_load_dwordx4 v[168:171], v[184:185], off offset:192
	global_load_dwordx4 v[172:175], v[186:187], off offset:128
	global_load_dwordx4 v[178:181], v[186:187], off offset:192
	s_branch .LBB0_1652

; DI unsigned ordkey(float f) { const unsigned u = __float_as_uint(f); return (u & 0x80000000u) ? ~u : (u | 0x80000000u); }
; #define CE_DESC(x, y) do { const unsigned mx_ = (x) > (y) ? (x) : (y); const unsigned mn_ = (x) > (y) ? (y) : (x); (x) = mx_; (y) = mn_; } while (0)
; DI void sort16_desc(unsigned (&a)[16]) {
; #pragma unroll
;   for (int k = 2; k <= 16; k <<= 1)
; #pragma unroll
;     for (int j = k >> 1; j > 0; j >>= 1)
; #pragma unroll
;       for (int i = 0; i < 16; ++i) {
;         const int l = i ^ j;
;         if (l > i) { if ((i & k) == 0) CE_DESC(a[i], a[l]); else CE_DESC(a[l], a[i]); }
;       }
; }
; DI void peer_select_unit(const Params& p, int unit, char* lds, const bf16x8 (&kb)[4][4]) {
;     ...
;     const int rr = pass * 32 + (tid >> 3), part = tid & 7;
;     unsigned a[16], bq[16];
;     const float* srow = sc + rr * 132 + 16 * part;
; #pragma unroll
;     for (int j = 0; j < 4; ++j) {
;       const f32x4 v = *(const f32x4*)(srow + 4 * j);
; #pragma unroll
;       for (int e = 0; e < 4; ++e) a[4 * j + e] = (ordkey(v[e]) & ~127u) | (unsigned)(127 - (16 * part + 4 * j + e));
;     }
;     sort16_desc(a);
.LBB0_1653:
	v_add_u32_e32 v71, s69, v64
	v_mul_lo_u32 v76, v71, s2
	v_add_u32_e32 v77, v68, v76
	ds_read_b128 v[78:81], v77
	ds_read_b128 v[82:85], v77 offset:16
	ds_read_b128 v[86:89], v77 offset:32
	ds_read_b128 v[90:93], v77 offset:48
	v_cndmask_b32_e64 v70, 0, 1, s[20:21]
	s_waitcnt lgkmcnt(3)
	v_not_b32_e32 v77, v78
	v_or_b32_e32 v94, 0x80000000, v78
	v_not_b32_e32 v95, v79
	v_or_b32_e32 v96, 0x80000000, v79
	v_cmp_gt_i32_e32 vcc, 0, v79
	v_not_b32_e32 v79, v80
	v_or_b32_e32 v97, 0x80000000, v80
	v_cmp_gt_i32_e64 s[20:21], 0, v80
	v_not_b32_e32 v80, v81
	v_or_b32_e32 v98, 0x80000000, v81
	v_cmp_gt_i32_e64 s[22:23], 0, v81
	s_waitcnt lgkmcnt(2)
	v_not_b32_e32 v81, v82
	v_or_b32_e32 v99, 0x80000000, v82
	v_cmp_gt_i32_e64 s[24:25], 0, v82
	v_not_b32_e32 v82, v83
	v_or_b32_e32 v100, 0x80000000, v83
	v_cmp_gt_i32_e64 s[26:27], 0, v83
	v_not_b32_e32 v83, v84
	v_or_b32_e32 v101, 0x80000000, v84
	v_cmp_gt_i32_e64 s[28:29], 0, v84
	v_not_b32_e32 v84, v85
	v_or_b32_e32 v102, 0x80000000, v85
	v_cmp_gt_i32_e64 s[30:31], 0, v85
	s_waitcnt lgkmcnt(1)
	v_not_b32_e32 v85, v86
	v_or_b32_e32 v103, 0x80000000, v86
	v_cmp_gt_i32_e64 s[34:35], 0, v86
	v_not_b32_e32 v86, v87
	v_or_b32_e32 v104, 0x80000000, v87
	v_cmp_gt_i32_e64 s[36:37], 0, v87
	v_not_b32_e32 v87, v88
	v_or_b32_e32 v105, 0x80000000, v88
	v_cmp_gt_i32_e64 s[38:39], 0, v88
	v_not_b32_e32 v88, v89
	v_or_b32_e32 v106, 0x80000000, v89
	v_cmp_gt_i32_e64 s[40:41], 0, v89
	s_waitcnt lgkmcnt(0)
	v_not_b32_e32 v89, v90
	v_or_b32_e32 v107, 0x80000000, v90
	v_cmp_gt_i32_e64 s[42:43], 0, v90
	v_not_b32_e32 v90, v91
	v_or_b32_e32 v108, 0x80000000, v91
	v_cmp_gt_i32_e64 s[44:45], 0, v91
	v_not_b32_e32 v91, v92
	v_or_b32_e32 v109, 0x80000000, v92
	v_cmp_gt_i32_e64 s[46:47], 0, v92
	v_not_b32_e32 v92, v93
	v_or_b32_e32 v110, 0x80000000, v93
	v_cmp_gt_i32_e64 s[48:49], 0, v93
	v_cmp_gt_i32_e64 s[50:51], 0, v78
	v_cndmask_b32_e32 v78, v96, v95, vcc
	v_cndmask_b32_e64 v79, v97, v79, s[20:21]
	v_cndmask_b32_e64 v77, v94, v77, s[50:51]
	v_cndmask_b32_e64 v80, v98, v80, s[22:23]
	v_cndmask_b32_e64 v81, v99, v81, s[24:25]
	v_cndmask_b32_e64 v82, v100, v82, s[26:27]
	v_cndmask_b32_e64 v83, v101, v83, s[28:29]
	v_cndmask_b32_e64 v84, v102, v84, s[30:31]
	v_cndmask_b32_e64 v85, v103, v85, s[34:35]
	v_cndmask_b32_e64 v86, v104, v86, s[36:37]
	v_cndmask_b32_e64 v87, v105, v87, s[38:39]
	v_cndmask_b32_e64 v88, v106, v88, s[40:41]
	v_cndmask_b32_e64 v89, v107, v89, s[42:43]
	v_cndmask_b32_e64 v90, v108, v90, s[44:45]
	v_cndmask_b32_e64 v91, v109, v91, s[46:47]
	v_cndmask_b32_e64 v92, v110, v92, s[48:49]
	v_and_b32_e32 v77, 0xffffff80, v77
	v_and_b32_e32 v78, 0xffffff80, v78
	v_and_b32_e32 v79, 0xffffff80, v79
	v_and_b32_e32 v80, 0xffffff80, v80
	v_and_b32_e32 v81, 0xffffff80, v81
	v_and_b32_e32 v82, 0xffffff80, v82
	v_and_b32_e32 v83, 0xffffff80, v83
	v_and_b32_e32 v84, 0xffffff80, v84
	v_and_b32_e32 v85, 0xffffff80, v85
	v_and_b32_e32 v86, 0xffffff80, v86
	v_and_b32_e32 v87, 0xffffff80, v87
	v_and_b32_e32 v88, 0xffffff80, v88
	v_and_b32_e32 v89, 0xffffff80, v89
	v_and_b32_e32 v90, 0xffffff80, v90
	v_and_b32_e32 v91, 0xffffff80, v91
	v_and_b32_e32 v92, 0xffffff80, v92
	v_sub_u32_e32 v77, v77, v67
	v_sub_u32_e32 v78, v78, v67
	v_sub_u32_e32 v79, v79, v67
	v_sub_u32_e32 v80, v80, v67
	v_sub_u32_e32 v81, v81, v67
	v_sub_u32_e32 v82, v82, v67
	v_sub_u32_e32 v83, v83, v67
	v_sub_u32_e32 v84, v84, v67
	v_sub_u32_e32 v85, v85, v67
	v_sub_u32_e32 v86, v86, v67
	v_sub_u32_e32 v87, v87, v67
	v_sub_u32_e32 v88, v88, v67
	v_sub_u32_e32 v89, v89, v67
	v_sub_u32_e32 v90, v90, v67
	v_sub_u32_e32 v91, v91, v67
	v_sub_u32_e32 v92, v92, v67
	v_add_u32_e32 v77, 0x7f, v77
	v_add_u32_e32 v78, 0x7e, v78
	v_add_u32_e32 v79, 0x7d, v79
	v_add_u32_e32 v80, 0x7c, v80
	v_add_u32_e32 v81, 0x7b, v81
	v_add_u32_e32 v82, 0x7a, v82
	v_add_u32_e32 v83, 0x79, v83
	v_add_u32_e32 v84, 0x78, v84
	v_add_u32_e32 v85, 0x77, v85
	v_add_u32_e32 v86, 0x76, v86
	v_add_u32_e32 v87, 0x75, v87
	v_add_u32_e32 v88, 0x74, v88
	v_add_u32_e32 v89, 0x73, v89
	v_add_u32_e32 v90, 0x72, v90
	v_add_u32_e32 v91, 0x71, v91
	v_add_u32_e32 v92, 0x70, v92
	v_max_u32_e32 v93, v77, v78
	v_min_u32_e32 v77, v77, v78
	v_max_u32_e32 v78, v80, v79
	v_min_u32_e32 v79, v80, v79
	v_max_u32_e32 v80, v81, v82
	v_min_u32_e32 v81, v81, v82
	v_max_u32_e32 v82, v84, v83
	v_min_u32_e32 v83, v84, v83
	v_max_u32_e32 v84, v85, v86
	v_min_u32_e32 v85, v85, v86
	v_max_u32_e32 v86, v88, v87
	v_min_u32_e32 v87, v88, v87
	v_max_u32_e32 v88, v89, v90
	v_min_u32_e32 v89, v89, v90
	v_max_u32_e32 v90, v92, v91
	v_min_u32_e32 v91, v92, v91
	v_max_u32_e32 v92, v93, v79
	v_min_u32_e32 v79, v93, v79
	v_max_u32_e32 v93, v77, v78
	v_min_u32_e32 v77, v77, v78
	v_max_u32_e32 v78, v83, v80
	v_min_u32_e32 v80, v83, v80
	v_max_u32_e32 v83, v82, v81
	v_min_u32_e32 v81, v82, v81
	v_max_u32_e32 v82, v84, v87
	v_min_u32_e32 v84, v84, v87
	v_max_u32_e32 v87, v85, v86
	v_min_u32_e32 v85, v85, v86
	v_max_u32_e32 v86, v91, v88
	v_min_u32_e32 v88, v91, v88
	v_max_u32_e32 v91, v90, v89
	v_min_u32_e32 v89, v90, v89
	v_max_u32_e32 v90, v92, v93
	v_min_u32_e32 v92, v92, v93
	v_max_u32_e32 v93, v79, v77
	v_min_u32_e32 v77, v79, v77
	v_max_u32_e32 v79, v81, v80
	v_min_u32_e32 v80, v81, v80
	v_max_u32_e32 v81, v83, v78
	v_min_u32_e32 v78, v83, v78
	v_max_u32_e32 v83, v82, v87
	v_min_u32_e32 v82, v82, v87
	v_max_u32_e32 v87, v84, v85
	v_min_u32_e32 v84, v84, v85
	v_max_u32_e32 v85, v89, v88
	v_min_u32_e32 v88, v89, v88
	v_max_u32_e32 v89, v91, v86
	v_min_u32_e32 v86, v91, v86
	v_max_u32_e32 v91, v90, v80
	v_min_u32_e32 v80, v90, v80
	v_max_u32_e32 v90, v92, v79
	v_min_u32_e32 v79, v92, v79
	v_max_u32_e32 v92, v93, v78
; #define CE_DESC(x, y) do { const unsigned mx_ = (x) > (y) ? (x) : (y); const unsigned mn_ = (x) > (y) ? (y) : (x); (x) = mx_; (y) = mn_; } while (0)
; DI void sort16_desc(unsigned (&a)[16]) {
; #pragma unroll
;   for (int k = 2; k <= 16; k <<= 1)
; #pragma unroll
;     for (int j = k >> 1; j > 0; j >>= 1)
; #pragma unroll
;       for (int i = 0; i < 16; ++i) {
;         const int l = i ^ j;
;         if (l > i) { if ((i & k) == 0) CE_DESC(a[i], a[l]); else CE_DESC(a[l], a[i]); }
;       }
; }
; DI void merge16_desc(unsigned (&a)[16], const unsigned (&b)[16]) {
; #pragma unroll
;   for (int i = 0; i < 16; ++i) a[i] = a[i] > b[15 - i] ? a[i] : b[15 - i];
; #pragma unroll
;   for (int j = 8; j > 0; j >>= 1)
; #pragma unroll
;     for (int i = 0; i < 16; ++i) if ((i & j) == 0) CE_DESC(a[i], a[i + j]);
; }
; template <int CTRL> DI void dpp16(unsigned (&b)[16], const unsigned (&a)[16]) {
; #pragma unroll
;   for (int s = 0; s < 16; ++s) b[s] = (unsigned)__builtin_amdgcn_update_dpp(0, (int)a[s], CTRL, 0xF, 0xF, true);
; }
	v_min_u32_e32 v78, v93, v78
	v_max_u32_e32 v93, v77, v81
	v_min_u32_e32 v77, v77, v81
	v_max_u32_e32 v81, v88, v83
	v_min_u32_e32 v83, v88, v83
	v_max_u32_e32 v88, v85, v82
	v_min_u32_e32 v82, v85, v82
	v_max_u32_e32 v85, v86, v87
	v_min_u32_e32 v86, v86, v87
	v_max_u32_e32 v87, v89, v84
	v_min_u32_e32 v84, v89, v84
	v_max_u32_e32 v89, v91, v92
	v_min_u32_e32 v91, v91, v92
	v_max_u32_e32 v92, v90, v93
	v_min_u32_e32 v90, v90, v93
	v_max_u32_e32 v93, v80, v78
	v_min_u32_e32 v78, v80, v78
	v_max_u32_e32 v80, v79, v77
	v_min_u32_e32 v77, v79, v77
	v_max_u32_e32 v79, v86, v83
	v_min_u32_e32 v83, v86, v83
	v_max_u32_e32 v86, v84, v82
	v_min_u32_e32 v82, v84, v82
	v_max_u32_e32 v84, v85, v81
	v_min_u32_e32 v81, v85, v81
	v_max_u32_e32 v85, v87, v88
	v_min_u32_e32 v87, v87, v88
	v_max_u32_e32 v88, v89, v92
	v_min_u32_e32 v89, v89, v92
	v_max_u32_e32 v92, v91, v90
	v_min_u32_e32 v90, v91, v90
	v_max_u32_e32 v91, v93, v80
	v_min_u32_e32 v80, v93, v80
	v_max_u32_e32 v93, v78, v77
	v_min_u32_e32 v77, v78, v77
	v_max_u32_e32 v78, v82, v83
	v_min_u32_e32 v82, v82, v83
	v_max_u32_e32 v83, v86, v79
	v_min_u32_e32 v79, v86, v79
	v_max_u32_e32 v86, v87, v81
	v_min_u32_e32 v81, v87, v81
	v_max_u32_e32 v87, v85, v84
	v_min_u32_e32 v84, v85, v84
	v_max_u32_e32 v85, v88, v82
	v_min_u32_e32 v82, v88, v82
	v_max_u32_e32 v88, v89, v78
	v_min_u32_e32 v78, v89, v78
	v_max_u32_e32 v89, v92, v79
	v_min_u32_e32 v79, v92, v79
	v_max_u32_e32 v92, v90, v83
	v_min_u32_e32 v83, v90, v83
	v_max_u32_e32 v90, v91, v81
	v_min_u32_e32 v81, v91, v81
	v_max_u32_e32 v91, v80, v86
	v_min_u32_e32 v80, v80, v86
	v_max_u32_e32 v86, v93, v84
	v_min_u32_e32 v84, v93, v84
	v_max_u32_e32 v93, v77, v87
	v_min_u32_e32 v77, v77, v87
	v_max_u32_e32 v87, v85, v90
	v_min_u32_e32 v85, v85, v90
	v_max_u32_e32 v90, v88, v91
	v_min_u32_e32 v88, v88, v91
	v_max_u32_e32 v91, v89, v86
	v_min_u32_e32 v86, v89, v86
	v_max_u32_e32 v89, v92, v93
	v_min_u32_e32 v92, v92, v93
	v_max_u32_e32 v93, v82, v81
	v_min_u32_e32 v81, v82, v81
	v_max_u32_e32 v82, v78, v80
	v_min_u32_e32 v78, v78, v80
	v_max_u32_e32 v80, v79, v84
	v_min_u32_e32 v79, v79, v84
	v_max_u32_e32 v84, v83, v77
	v_min_u32_e32 v77, v83, v77
	v_max_u32_e32 v83, v87, v91
	v_min_u32_e32 v87, v87, v91
	v_max_u32_e32 v91, v90, v89
	v_min_u32_e32 v89, v90, v89
	v_max_u32_e32 v90, v85, v86
	v_min_u32_e32 v85, v85, v86
	v_max_u32_e32 v86, v88, v92
	v_min_u32_e32 v88, v88, v92
	v_max_u32_e32 v92, v93, v80
	v_min_u32_e32 v80, v93, v80
	v_max_u32_e32 v93, v82, v84
	v_min_u32_e32 v82, v82, v84
	v_max_u32_e32 v84, v81, v79
	v_min_u32_e32 v79, v81, v79
	v_max_u32_e32 v81, v78, v77
	v_min_u32_e32 v77, v78, v77
	v_max_u32_e32 v78, v83, v91
	v_min_u32_e32 v83, v83, v91
	v_max_u32_e32 v91, v87, v89
	v_min_u32_e32 v87, v87, v89
	v_max_u32_e32 v89, v90, v86
	v_min_u32_e32 v86, v90, v86
	v_max_u32_e32 v90, v85, v88
	v_min_u32_e32 v85, v85, v88
	v_max_u32_e32 v88, v92, v93
	v_min_u32_e32 v92, v92, v93
	v_max_u32_e32 v93, v80, v82
	v_min_u32_e32 v80, v80, v82
	v_max_u32_e32 v82, v84, v81
	v_min_u32_e32 v81, v84, v81
	v_max_u32_e32 v84, v79, v77
	v_min_u32_e32 v77, v79, v77
	v_mov_b32_dpp v79, v78 quad_perm:[1,0,3,2] row_mask:0xf bank_mask:0xf bound_ctrl:1
	v_mov_b32_dpp v94, v83 quad_perm:[1,0,3,2] row_mask:0xf bank_mask:0xf bound_ctrl:1
	v_mov_b32_dpp v95, v91 quad_perm:[1,0,3,2] row_mask:0xf bank_mask:0xf bound_ctrl:1
	v_mov_b32_dpp v96, v87 quad_perm:[1,0,3,2] row_mask:0xf bank_mask:0xf bound_ctrl:1
	v_mov_b32_dpp v97, v89 quad_perm:[1,0,3,2] row_mask:0xf bank_mask:0xf bound_ctrl:1
	v_mov_b32_dpp v98, v86 quad_perm:[1,0,3,2] row_mask:0xf bank_mask:0xf bound_ctrl:1
	v_max_u32_dpp v78, v77, v78 quad_perm:[1,0,3,2] row_mask:0xf bank_mask:0xf bound_ctrl:1
	v_max_u32_dpp v83, v84, v83 quad_perm:[1,0,3,2] row_mask:0xf bank_mask:0xf bound_ctrl:1
	v_max_u32_dpp v91, v81, v91 quad_perm:[1,0,3,2] row_mask:0xf bank_mask:0xf bound_ctrl:1
	v_max_u32_dpp v87, v82, v87 quad_perm:[1,0,3,2] row_mask:0xf bank_mask:0xf bound_ctrl:1
	v_max_u32_dpp v89, v80, v89 quad_perm:[1,0,3,2] row_mask:0xf bank_mask:0xf bound_ctrl:1
	v_max_u32_dpp v86, v93, v86 quad_perm:[1,0,3,2] row_mask:0xf bank_mask:0xf bound_ctrl:1
	v_max_u32_dpp v99, v92, v90 quad_perm:[1,0,3,2] row_mask:0xf bank_mask:0xf bound_ctrl:1
	v_max_u32_dpp v100, v88, v85 quad_perm:[1,0,3,2] row_mask:0xf bank_mask:0xf bound_ctrl:1
	v_max_u32_dpp v85, v85, v88 quad_perm:[1,0,3,2] row_mask:0xf bank_mask:0xf bound_ctrl:1
	v_max_u32_dpp v88, v90, v92 quad_perm:[1,0,3,2] row_mask:0xf bank_mask:0xf bound_ctrl:1
	v_max_u32_e32 v90, v93, v98
	v_max_u32_e32 v80, v80, v97
	v_max_u32_e32 v82, v82, v96
	v_max_u32_e32 v81, v81, v95
	v_max_u32_e32 v84, v84, v94
	v_max_u32_e32 v77, v77, v79
	v_max_u32_e32 v79, v78, v85
	v_min_u32_e32 v78, v78, v85
	v_max_u32_e32 v85, v83, v88
	v_min_u32_e32 v83, v83, v88
	v_max_u32_e32 v88, v91, v90
	v_min_u32_e32 v90, v91, v90
	v_max_u32_e32 v91, v87, v80
	v_min_u32_e32 v80, v87, v80
	v_max_u32_e32 v87, v89, v82
	v_min_u32_e32 v82, v89, v82
	v_max_u32_e32 v89, v86, v81
	v_min_u32_e32 v81, v86, v81
	v_max_u32_e32 v86, v99, v84
	v_max_u32_e32 v92, v100, v77
	v_min_u32_e32 v84, v99, v84
	v_min_u32_e32 v77, v100, v77
	v_max_u32_e32 v93, v79, v87
	v_min_u32_e32 v79, v79, v87
	v_max_u32_e32 v87, v85, v89
	v_min_u32_e32 v85, v85, v89
	v_max_u32_e32 v89, v88, v86
	v_min_u32_e32 v86, v88, v86
	v_max_u32_e32 v88, v91, v92
	v_min_u32_e32 v91, v91, v92
	v_max_u32_e32 v92, v78, v82
	v_min_u32_e32 v78, v78, v82
	v_max_u32_e32 v82, v83, v81
	v_min_u32_e32 v81, v83, v81
	v_max_u32_e32 v83, v90, v84
	v_min_u32_e32 v84, v90, v84
	v_max_u32_e32 v90, v80, v77
	v_min_u32_e32 v77, v80, v77
	v_max_u32_e32 v80, v93, v89
; #define CE_DESC(x, y) do { const unsigned mx_ = (x) > (y) ? (x) : (y); const unsigned mn_ = (x) > (y) ? (y) : (x); (x) = mx_; (y) = mn_; } while (0)
; DI void merge16_desc(unsigned (&a)[16], const unsigned (&b)[16]) {
; #pragma unroll
;   for (int i = 0; i < 16; ++i) a[i] = a[i] > b[15 - i] ? a[i] : b[15 - i];
; #pragma unroll
;   for (int j = 8; j > 0; j >>= 1)
; #pragma unroll
;     for (int i = 0; i < 16; ++i) if ((i & j) == 0) CE_DESC(a[i], a[i + j]);
; }
; template <int CTRL> DI void dpp16(unsigned (&b)[16], const unsigned (&a)[16]) {
; #pragma unroll
;   for (int s = 0; s < 16; ++s) b[s] = (unsigned)__builtin_amdgcn_update_dpp(0, (int)a[s], CTRL, 0xF, 0xF, true);
; }
	v_min_u32_e32 v89, v93, v89
	v_max_u32_e32 v93, v87, v88
	v_min_u32_e32 v87, v87, v88
	v_max_u32_e32 v88, v79, v86
	v_min_u32_e32 v79, v79, v86
	v_max_u32_e32 v86, v85, v91
	v_min_u32_e32 v85, v85, v91
	v_max_u32_e32 v91, v92, v83
	v_min_u32_e32 v83, v92, v83
	v_max_u32_e32 v92, v82, v90
	v_min_u32_e32 v82, v82, v90
	v_max_u32_e32 v90, v78, v84
	v_min_u32_e32 v78, v78, v84
	v_max_u32_e32 v84, v81, v77
	v_min_u32_e32 v77, v81, v77
	v_max_u32_e32 v81, v80, v93
	v_min_u32_e32 v80, v80, v93
	v_max_u32_e32 v93, v89, v87
	v_min_u32_e32 v87, v89, v87
	v_max_u32_e32 v89, v88, v86
	v_min_u32_e32 v86, v88, v86
	v_max_u32_e32 v88, v79, v85
	v_min_u32_e32 v79, v79, v85
	v_max_u32_e32 v85, v91, v92
	v_min_u32_e32 v91, v91, v92
	v_max_u32_e32 v92, v83, v82
	v_min_u32_e32 v82, v83, v82
	v_max_u32_e32 v83, v90, v84
	v_min_u32_e32 v84, v90, v84
	v_max_u32_e32 v90, v78, v77
	v_min_u32_e32 v77, v78, v77
	v_mov_b32_dpp v78, v81 quad_perm:[2,3,0,1] row_mask:0xf bank_mask:0xf bound_ctrl:1
	v_mov_b32_dpp v94, v80 quad_perm:[2,3,0,1] row_mask:0xf bank_mask:0xf bound_ctrl:1
	v_mov_b32_dpp v95, v93 quad_perm:[2,3,0,1] row_mask:0xf bank_mask:0xf bound_ctrl:1
	v_mov_b32_dpp v96, v87 quad_perm:[2,3,0,1] row_mask:0xf bank_mask:0xf bound_ctrl:1
	v_mov_b32_dpp v97, v89 quad_perm:[2,3,0,1] row_mask:0xf bank_mask:0xf bound_ctrl:1
	v_mov_b32_dpp v98, v86 quad_perm:[2,3,0,1] row_mask:0xf bank_mask:0xf bound_ctrl:1
	v_max_u32_dpp v81, v77, v81 quad_perm:[2,3,0,1] row_mask:0xf bank_mask:0xf bound_ctrl:1
	v_max_u32_dpp v80, v90, v80 quad_perm:[2,3,0,1] row_mask:0xf bank_mask:0xf bound_ctrl:1
	v_max_u32_dpp v93, v84, v93 quad_perm:[2,3,0,1] row_mask:0xf bank_mask:0xf bound_ctrl:1
	v_max_u32_dpp v87, v83, v87 quad_perm:[2,3,0,1] row_mask:0xf bank_mask:0xf bound_ctrl:1
	v_max_u32_dpp v89, v82, v89 quad_perm:[2,3,0,1] row_mask:0xf bank_mask:0xf bound_ctrl:1
	v_max_u32_dpp v86, v92, v86 quad_perm:[2,3,0,1] row_mask:0xf bank_mask:0xf bound_ctrl:1
	v_max_u32_dpp v99, v91, v88 quad_perm:[2,3,0,1] row_mask:0xf bank_mask:0xf bound_ctrl:1
	v_max_u32_dpp v100, v85, v79 quad_perm:[2,3,0,1] row_mask:0xf bank_mask:0xf bound_ctrl:1
	v_max_u32_dpp v79, v79, v85 quad_perm:[2,3,0,1] row_mask:0xf bank_mask:0xf bound_ctrl:1
	v_max_u32_dpp v85, v88, v91 quad_perm:[2,3,0,1] row_mask:0xf bank_mask:0xf bound_ctrl:1
	v_max_u32_e32 v88, v92, v98
	v_max_u32_e32 v82, v82, v97
	v_max_u32_e32 v83, v83, v96
	v_max_u32_e32 v84, v84, v95
	v_max_u32_e32 v90, v90, v94
	v_max_u32_e32 v77, v77, v78
	v_max_u32_e32 v78, v81, v79
	v_min_u32_e32 v79, v81, v79
	v_max_u32_e32 v81, v80, v85
	v_min_u32_e32 v80, v80, v85
	v_max_u32_e32 v85, v93, v88
	v_max_u32_e32 v91, v87, v82
	v_min_u32_e32 v82, v87, v82
	v_max_u32_e32 v87, v89, v83
	v_min_u32_e32 v83, v89, v83
	v_max_u32_e32 v89, v86, v84
	v_min_u32_e32 v84, v86, v84
	v_max_u32_e32 v86, v99, v90
	v_max_u32_e32 v92, v100, v77
	v_min_u32_e32 v88, v93, v88
	v_min_u32_e32 v90, v99, v90
	v_min_u32_e32 v77, v100, v77
	v_max_u32_e32 v93, v78, v87
	v_min_u32_e32 v78, v78, v87
	v_max_u32_e32 v87, v81, v89
	v_min_u32_e32 v81, v81, v89
	v_max_u32_e32 v89, v85, v86
	v_min_u32_e32 v85, v85, v86
	v_max_u32_e32 v86, v91, v92
	v_min_u32_e32 v91, v91, v92
	v_max_u32_e32 v92, v79, v83
	v_min_u32_e32 v79, v79, v83
	v_max_u32_e32 v83, v80, v84
	v_min_u32_e32 v80, v80, v84
	v_max_u32_e32 v84, v88, v90
	v_min_u32_e32 v88, v88, v90
	v_max_u32_e32 v90, v82, v77
	v_min_u32_e32 v77, v82, v77
	v_max_u32_e32 v82, v93, v89
	v_min_u32_e32 v89, v93, v89
	v_max_u32_e32 v93, v87, v86
	v_min_u32_e32 v86, v87, v86
	v_max_u32_e32 v87, v78, v85
	v_min_u32_e32 v78, v78, v85
	v_max_u32_e32 v85, v81, v91
	v_min_u32_e32 v81, v81, v91
	v_max_u32_e32 v91, v92, v84
	v_min_u32_e32 v84, v92, v84
	v_max_u32_e32 v92, v83, v90
	v_min_u32_e32 v83, v83, v90
	v_max_u32_e32 v90, v79, v88
	v_min_u32_e32 v79, v79, v88
	v_max_u32_e32 v88, v80, v77
	v_min_u32_e32 v77, v80, v77
	v_max_u32_e32 v80, v82, v93
	v_min_u32_e32 v82, v82, v93
	v_max_u32_e32 v93, v89, v86
	v_min_u32_e32 v86, v89, v86
	v_max_u32_e32 v89, v87, v85
	v_min_u32_e32 v85, v87, v85
	v_max_u32_e32 v87, v78, v81
	v_min_u32_e32 v78, v78, v81
	v_max_u32_e32 v81, v91, v92
	v_min_u32_e32 v91, v91, v92
	v_max_u32_e32 v92, v84, v83
	v_min_u32_e32 v83, v84, v83
	v_max_u32_e32 v84, v90, v88
	v_min_u32_e32 v88, v90, v88
	v_max_u32_e32 v90, v79, v77
	v_min_u32_e32 v77, v79, v77
	v_mov_b32_dpp v79, v80 row_half_mirror row_mask:0xf bank_mask:0xf bound_ctrl:1
	v_mov_b32_dpp v94, v82 row_half_mirror row_mask:0xf bank_mask:0xf bound_ctrl:1
	v_mov_b32_dpp v95, v93 row_half_mirror row_mask:0xf bank_mask:0xf bound_ctrl:1
	v_mov_b32_dpp v96, v86 row_half_mirror row_mask:0xf bank_mask:0xf bound_ctrl:1
	v_mov_b32_dpp v97, v89 row_half_mirror row_mask:0xf bank_mask:0xf bound_ctrl:1
	v_mov_b32_dpp v98, v85 row_half_mirror row_mask:0xf bank_mask:0xf bound_ctrl:1
	v_max_u32_dpp v80, v77, v80 row_half_mirror row_mask:0xf bank_mask:0xf bound_ctrl:1
	v_max_u32_dpp v82, v90, v82 row_half_mirror row_mask:0xf bank_mask:0xf bound_ctrl:1
	v_max_u32_dpp v93, v88, v93 row_half_mirror row_mask:0xf bank_mask:0xf bound_ctrl:1
	v_max_u32_dpp v86, v84, v86 row_half_mirror row_mask:0xf bank_mask:0xf bound_ctrl:1
	v_max_u32_dpp v89, v83, v89 row_half_mirror row_mask:0xf bank_mask:0xf bound_ctrl:1
	v_max_u32_dpp v85, v92, v85 row_half_mirror row_mask:0xf bank_mask:0xf bound_ctrl:1
	v_max_u32_dpp v99, v91, v87 row_half_mirror row_mask:0xf bank_mask:0xf bound_ctrl:1
	v_max_u32_dpp v100, v81, v78 row_half_mirror row_mask:0xf bank_mask:0xf bound_ctrl:1
	v_max_u32_dpp v78, v78, v81 row_half_mirror row_mask:0xf bank_mask:0xf bound_ctrl:1
	v_max_u32_dpp v81, v87, v91 row_half_mirror row_mask:0xf bank_mask:0xf bound_ctrl:1
; DI unsigned ordkey(float f) { const unsigned u = __float_as_uint(f); return (u & 0x80000000u) ? ~u : (u | 0x80000000u); }
; DI void peer_select_unit(const Params& p, int unit, char* lds, const bf16x8 (&kb)[4][4]) {
;     ...
;     dpp16<0x141>(bq, a); merge16_desc(a, bq);
; #pragma unroll
;     for (int s = 0; s < 2; ++s) {
;       unsigned k = 0u;
; #pragma unroll
;       for (int q = 0; q < 8; ++q) k = part == q ? a[2 * q + s] : k;
;       const int idx = 127 - (int)(k & 127u);
;       topv[rr * 16 + 2 * part + s] = sc[rr * 132 + idx]; topi[rr * 16 + 2 * part + s] = idx;
;     }
;   }
;   __syncthreads();
;   if (tid < 128) {
;     const int tok = tid >> 2, q4 = tid & 3;
;     unsigned c[16], bq[16];
; #pragma unroll
;     for (int i = 0; i < 16; ++i) {
;       const unsigned code = PEER_CAND[16 * q4 + i];
;       const float v = topv[tok * 16 + ((code >> 4) & 15)] + topv[(32 + tok) * 16 + (code & 15)];
;       c[i] = code == 0xFFu ? 0u : ((ordkey(v) & ~255u) | (255u - code));
	v_max_u32_e32 v87, v92, v98
	v_max_u32_e32 v83, v83, v97
	v_max_u32_e32 v84, v84, v96
	v_max_u32_e32 v88, v88, v95
	v_max_u32_e32 v90, v90, v94
	v_max_u32_e32 v77, v77, v79
	v_max_u32_e32 v79, v80, v78
	v_min_u32_e32 v78, v80, v78
	v_max_u32_e32 v80, v82, v81
	v_min_u32_e32 v81, v82, v81
	v_max_u32_e32 v82, v93, v87
	v_max_u32_e32 v91, v86, v83
	v_min_u32_e32 v83, v86, v83
	v_max_u32_e32 v86, v89, v84
	v_min_u32_e32 v84, v89, v84
	v_max_u32_e32 v89, v85, v88
	v_min_u32_e32 v85, v85, v88
	v_max_u32_e32 v88, v99, v90
	v_max_u32_e32 v92, v100, v77
	v_min_u32_e32 v87, v93, v87
	v_min_u32_e32 v90, v99, v90
	v_min_u32_e32 v77, v100, v77
	v_max_u32_e32 v93, v79, v86
	v_min_u32_e32 v79, v79, v86
	v_max_u32_e32 v86, v80, v89
	v_min_u32_e32 v80, v80, v89
	v_max_u32_e32 v89, v82, v88
	v_min_u32_e32 v82, v82, v88
	v_max_u32_e32 v88, v91, v92
	v_min_u32_e32 v91, v91, v92
	v_max_u32_e32 v92, v78, v84
	v_min_u32_e32 v78, v78, v84
	v_max_u32_e32 v84, v81, v85
	v_min_u32_e32 v81, v81, v85
	v_max_u32_e32 v85, v87, v90
	v_min_u32_e32 v87, v87, v90
	v_max_u32_e32 v90, v83, v77
	v_min_u32_e32 v77, v83, v77
	v_max_u32_e32 v83, v93, v89
	v_min_u32_e32 v89, v93, v89
	v_max_u32_e32 v93, v86, v88
	v_min_u32_e32 v86, v86, v88
	v_max_u32_e32 v88, v79, v82
	v_min_u32_e32 v79, v79, v82
	v_max_u32_e32 v82, v80, v91
	v_min_u32_e32 v80, v80, v91
	v_max_u32_e32 v91, v92, v85
	v_min_u32_e32 v85, v92, v85
	v_max_u32_e32 v92, v84, v90
	v_min_u32_e32 v84, v84, v90
	v_max_u32_e32 v90, v78, v87
	v_min_u32_e32 v78, v78, v87
	v_max_u32_e32 v87, v81, v77
	v_min_u32_e32 v77, v81, v77
	v_max_u32_e32 v81, v83, v93
	v_min_u32_e32 v83, v83, v93
	v_max_u32_e32 v93, v89, v86
	v_min_u32_e32 v86, v89, v86
	v_max_u32_e32 v89, v88, v82
	v_min_u32_e32 v82, v88, v82
	v_max_u32_e32 v88, v79, v80
	v_min_u32_e32 v79, v79, v80
	v_max_u32_e32 v80, v91, v92
	v_min_u32_e32 v91, v91, v92
	v_max_u32_e32 v92, v85, v84
	v_min_u32_e32 v84, v85, v84
	v_max_u32_e32 v85, v90, v87
	v_min_u32_e32 v87, v90, v87
	v_max_u32_e32 v90, v78, v77
	v_min_u32_e32 v77, v78, v77
	v_cndmask_b32_e64 v78, 0, v81, s[0:1]
	v_cndmask_b32_e64 v78, v78, v93, s[4:5]
	v_cndmask_b32_e64 v78, v78, v89, s[6:7]
	v_cndmask_b32_e64 v78, v78, v88, s[8:9]
	v_cndmask_b32_e64 v78, v78, v80, s[10:11]
	v_cndmask_b32_e64 v78, v78, v92, s[12:13]
	v_cndmask_b32_e64 v81, 0, v83, s[0:1]
	v_cndmask_b32_e64 v78, v78, v85, s[14:15]
	v_cndmask_b32_e64 v81, v81, v86, s[4:5]
	v_cndmask_b32_e64 v78, v78, v90, s[16:17]
	v_cndmask_b32_e64 v81, v81, v82, s[6:7]
	v_bitop3_b32 v78, v78, s3, v78 bitop3:0xc
	v_cndmask_b32_e64 v79, v81, v79, s[8:9]
	v_lshlrev_b32_e32 v80, 2, v78
	v_cndmask_b32_e64 v79, v79, v91, s[10:11]
	v_add3_u32 v80, v146, v80, v76
	v_cndmask_b32_e64 v79, v79, v84, s[12:13]
	ds_read_b32 v80, v80
	v_cndmask_b32_e64 v79, v79, v87, s[14:15]
	v_cndmask_b32_e64 v77, v79, v77, s[16:17]
	v_lshl_or_b32 v71, v71, 6, v69
	v_bitop3_b32 v79, v77, s3, v77 bitop3:0xc
	v_add_u32_e32 v71, v146, v71
	v_lshlrev_b32_e32 v77, 2, v79
	v_add3_u32 v76, v146, v77, v76
	s_waitcnt lgkmcnt(0)
	ds_write_b32 v71, v80 offset:33792
	ds_read_b32 v76, v76
	v_cmp_ne_u32_e32 vcc, 1, v70
	s_mov_b32 s69, 32
	s_mov_b64 s[20:21], 0
	ds_write_b64 v71, v[78:79] offset:37888
	s_waitcnt lgkmcnt(1)
	ds_write_b32 v71, v76 offset:33796
	s_cbranch_vccz .LBB0_1653
	v_cmp_gt_i32_e32 vcc, s18, v66
	s_waitcnt lgkmcnt(0)
	s_barrier
	s_and_saveexec_b64 s[8:9], vcc
	s_cbranch_execz .LBB0_1651
	v_and_b32_e32 v77, 3, v66
	v_lshlrev_b32_e32 v64, 4, v77
	v_and_b32_e32 v80, 0xffff, v244
	v_lshlrev_b32_e32 v66, 6, v75
	v_lshlrev_b32_e32 v76, 4, v75
	v_cmp_eq_u32_e32 vcc, 3, v77
	v_cmp_ne_u32_e64 s[0:1], 3, v77
	v_mov_b32_e32 v82, 0
	v_lshrrev_b32_e32 v67, 2, v80
	v_and_b32_e32 v68, 15, v80
	v_lshrrev_b16_e32 v79, 8, v80
	v_and_b32_e32 v67, 60, v67
	v_lshlrev_b32_e32 v68, 2, v68
	v_lshrrev_b32_e32 v69, 2, v79
	v_and_b32_e32 v78, 15, v79
	v_add3_u32 v67, v146, v67, v66
	v_add3_u32 v68, v146, v68, v66
	v_and_b32_e32 v69, 60, v69
	v_lshlrev_b32_e32 v78, 2, v78
	v_add3_u32 v81, v146, v69, v66
	v_add3_u32 v78, v146, v78, v66
	ds_read_b32 v67, v67 offset:33792
	ds_read_b32 v69, v68 offset:35840
	ds_read_b32 v66, v81 offset:33792
	ds_read_b32 v68, v78 offset:35840
	v_mov_b32_e32 v81, 0
	v_lshlrev_b32_e32 v78, 2, v76
	v_mov_b32_e32 v83, 0
	v_mov_b32_e32 v84, 0
	v_mov_b32_e32 v85, 0
	v_mov_b32_e32 v86, 0
	v_mov_b32_e32 v87, 0
	v_mov_b32_e32 v88, 0
	v_mov_b32_e32 v89, 0
	v_mov_b32_e32 v90, 0
	v_mov_b32_e32 v91, 0
	v_mov_b32_e32 v92, 0
	v_mov_b32_e32 v93, 0
	v_mov_b32_e32 v94, 0
	s_and_saveexec_b64 s[6:7], s[0:1]
	v_bfe_u32 v82, v244, 16, 8
	v_lshrrev_b32_e32 v238, 2, v82
	v_and_b32_e32 v239, 15, v82
	v_and_b32_e32 v238, 60, v238
	v_lshlrev_b32_e32 v239, 2, v239
	v_add3_u32 v238, v146, v238, v78
	v_add3_u32 v239, v146, v239, v78
	ds_read_b32 v210, v238 offset:33792
	ds_read_b32 v211, v239 offset:35840
	v_bfe_u32 v81, v244, 24, 8
	v_lshrrev_b32_e32 v238, 2, v81
	v_and_b32_e32 v239, 15, v81
	v_and_b32_e32 v238, 60, v238
	v_lshlrev_b32_e32 v239, 2, v239
	v_add3_u32 v238, v146, v238, v78
	v_add3_u32 v239, v146, v239, v78
	ds_read_b32 v212, v238 offset:33792
	ds_read_b32 v213, v239 offset:35840
	v_bfe_u32 v84, v245, 0, 8
	v_lshrrev_b32_e32 v238, 2, v84
	v_and_b32_e32 v239, 15, v84
	v_and_b32_e32 v238, 60, v238
	v_lshlrev_b32_e32 v239, 2, v239
	v_add3_u32 v238, v146, v238, v78
	v_add3_u32 v239, v146, v239, v78
	ds_read_b32 v214, v238 offset:33792
	ds_read_b32 v215, v239 offset:35840
	v_bfe_u32 v83, v245, 8, 8
	v_lshrrev_b32_e32 v238, 2, v83
	v_and_b32_e32 v239, 15, v83
	v_and_b32_e32 v238, 60, v238
	v_lshlrev_b32_e32 v239, 2, v239
	v_add3_u32 v238, v146, v238, v78
	v_add3_u32 v239, v146, v239, v78
; DI unsigned ordkey(float f) { const unsigned u = __float_as_uint(f); return (u & 0x80000000u) ? ~u : (u | 0x80000000u); }
; DI void peer_select_unit(const Params& p, int unit, char* lds, const bf16x8 (&kb)[4][4]) {
;     ...
; #pragma unroll
;     for (int i = 0; i < 16; ++i) {
;       const unsigned code = PEER_CAND[16 * q4 + i];
;       const float v = topv[tok * 16 + ((code >> 4) & 15)] + topv[(32 + tok) * 16 + (code & 15)];
;       c[i] = code == 0xFFu ? 0u : ((ordkey(v) & ~255u) | (255u - code));
	ds_read_b32 v216, v238 offset:33792
	ds_read_b32 v217, v239 offset:35840
	v_bfe_u32 v86, v245, 16, 8
	v_lshrrev_b32_e32 v238, 2, v86
	v_and_b32_e32 v239, 15, v86
	v_and_b32_e32 v238, 60, v238
	v_lshlrev_b32_e32 v239, 2, v239
	v_add3_u32 v238, v146, v238, v78
	v_add3_u32 v239, v146, v239, v78
	ds_read_b32 v218, v238 offset:33792
	ds_read_b32 v219, v239 offset:35840
	v_bfe_u32 v85, v245, 24, 8
	v_lshrrev_b32_e32 v238, 2, v85
	v_and_b32_e32 v239, 15, v85
	v_and_b32_e32 v238, 60, v238
	v_lshlrev_b32_e32 v239, 2, v239
	v_add3_u32 v238, v146, v238, v78
	v_add3_u32 v239, v146, v239, v78
	ds_read_b32 v220, v238 offset:33792
	ds_read_b32 v221, v239 offset:35840
	v_bfe_u32 v88, v246, 0, 8
	v_lshrrev_b32_e32 v238, 2, v88
	v_and_b32_e32 v239, 15, v88
	v_and_b32_e32 v238, 60, v238
	v_lshlrev_b32_e32 v239, 2, v239
	v_add3_u32 v238, v146, v238, v78
	v_add3_u32 v239, v146, v239, v78
	ds_read_b32 v222, v238 offset:33792
	ds_read_b32 v223, v239 offset:35840
	v_bfe_u32 v87, v246, 8, 8
	v_lshrrev_b32_e32 v238, 2, v87
	v_and_b32_e32 v239, 15, v87
	v_and_b32_e32 v238, 60, v238
	v_lshlrev_b32_e32 v239, 2, v239
	v_add3_u32 v238, v146, v238, v78
	v_add3_u32 v239, v146, v239, v78
	ds_read_b32 v224, v238 offset:33792
	ds_read_b32 v225, v239 offset:35840
	v_bfe_u32 v90, v246, 16, 8
	v_lshrrev_b32_e32 v238, 2, v90
	v_and_b32_e32 v239, 15, v90
	v_and_b32_e32 v238, 60, v238
	v_lshlrev_b32_e32 v239, 2, v239
	v_add3_u32 v238, v146, v238, v78
	v_add3_u32 v239, v146, v239, v78
	ds_read_b32 v226, v238 offset:33792
	ds_read_b32 v227, v239 offset:35840
	v_bfe_u32 v89, v246, 24, 8
	v_lshrrev_b32_e32 v238, 2, v89
	v_and_b32_e32 v239, 15, v89
	v_and_b32_e32 v238, 60, v238
	v_lshlrev_b32_e32 v239, 2, v239
	v_add3_u32 v238, v146, v238, v78
	v_add3_u32 v239, v146, v239, v78
	ds_read_b32 v228, v238 offset:33792
	ds_read_b32 v229, v239 offset:35840
	v_bfe_u32 v92, v247, 0, 8
	v_lshrrev_b32_e32 v238, 2, v92
	v_and_b32_e32 v239, 15, v92
	v_and_b32_e32 v238, 60, v238
	v_lshlrev_b32_e32 v239, 2, v239
	v_add3_u32 v238, v146, v238, v78
	v_add3_u32 v239, v146, v239, v78
	ds_read_b32 v230, v238 offset:33792
	ds_read_b32 v231, v239 offset:35840
	v_bfe_u32 v91, v247, 8, 8
	v_lshrrev_b32_e32 v238, 2, v91
	v_and_b32_e32 v239, 15, v91
	v_and_b32_e32 v238, 60, v238
	v_lshlrev_b32_e32 v239, 2, v239
	v_add3_u32 v238, v146, v238, v78
	v_add3_u32 v239, v146, v239, v78
	ds_read_b32 v232, v238 offset:33792
	ds_read_b32 v233, v239 offset:35840
	v_bfe_u32 v94, v247, 16, 8
	v_lshrrev_b32_e32 v238, 2, v94
	v_and_b32_e32 v239, 15, v94
	v_and_b32_e32 v238, 60, v238
	v_lshlrev_b32_e32 v239, 2, v239
	v_add3_u32 v238, v146, v238, v78
	v_add3_u32 v239, v146, v239, v78
	ds_read_b32 v234, v238 offset:33792
	ds_read_b32 v235, v239 offset:35840
	v_bfe_u32 v70, v247, 24, 8
	v_lshrrev_b32_e32 v238, 2, v70
	v_and_b32_e32 v239, 15, v70
	v_and_b32_e32 v238, 60, v238
	v_lshlrev_b32_e32 v239, 2, v239
	v_add3_u32 v238, v146, v238, v78
	v_add3_u32 v239, v146, v239, v78
	ds_read_b32 v236, v238 offset:33792
	ds_read_b32 v237, v239 offset:35840
	s_waitcnt lgkmcnt(0)
	v_add_f32_e32 v210, v210, v211
	v_cmp_gt_i32_e64 s[4:5], 0, v210
	v_not_b32_e32 v211, v210
	v_or_b32_e32 v238, 0x80000000, v210
	v_cndmask_b32_e64 v210, v238, v211, s[4:5]
	v_and_b32_e32 v210, 0xffffff00, v210
	v_bitop3_b32 v82, v210, s19, v82 bitop3:0x36
	v_add_f32_e32 v212, v212, v213
	v_cmp_gt_i32_e64 s[4:5], 0, v212
	v_not_b32_e32 v213, v212
	v_or_b32_e32 v238, 0x80000000, v212
	v_cndmask_b32_e64 v212, v238, v213, s[4:5]
	v_and_b32_e32 v212, 0xffffff00, v212
	v_bitop3_b32 v81, v212, s19, v81 bitop3:0x36
	v_add_f32_e32 v214, v214, v215
	v_cmp_gt_i32_e64 s[4:5], 0, v214
	v_not_b32_e32 v215, v214
	v_or_b32_e32 v238, 0x80000000, v214
	v_cndmask_b32_e64 v214, v238, v215, s[4:5]
	v_and_b32_e32 v214, 0xffffff00, v214
	v_bitop3_b32 v84, v214, s19, v84 bitop3:0x36
	v_add_f32_e32 v216, v216, v217
	v_cmp_gt_i32_e64 s[4:5], 0, v216
	v_not_b32_e32 v217, v216
	v_or_b32_e32 v238, 0x80000000, v216
	v_cndmask_b32_e64 v216, v238, v217, s[4:5]
	v_and_b32_e32 v216, 0xffffff00, v216
	v_bitop3_b32 v83, v216, s19, v83 bitop3:0x36
	v_add_f32_e32 v218, v218, v219
	v_cmp_gt_i32_e64 s[4:5], 0, v218
	v_not_b32_e32 v219, v218
	v_or_b32_e32 v238, 0x80000000, v218
	v_cndmask_b32_e64 v218, v238, v219, s[4:5]
	v_and_b32_e32 v218, 0xffffff00, v218
	v_bitop3_b32 v86, v218, s19, v86 bitop3:0x36
	v_add_f32_e32 v220, v220, v221
	v_cmp_gt_i32_e64 s[4:5], 0, v220
	v_not_b32_e32 v221, v220
	v_or_b32_e32 v238, 0x80000000, v220
	v_cndmask_b32_e64 v220, v238, v221, s[4:5]
	v_and_b32_e32 v220, 0xffffff00, v220
	v_bitop3_b32 v85, v220, s19, v85 bitop3:0x36
	v_add_f32_e32 v222, v222, v223
	v_cmp_gt_i32_e64 s[4:5], 0, v222
	v_not_b32_e32 v223, v222
	v_or_b32_e32 v238, 0x80000000, v222
	v_cndmask_b32_e64 v222, v238, v223, s[4:5]
	v_and_b32_e32 v222, 0xffffff00, v222
	v_bitop3_b32 v88, v222, s19, v88 bitop3:0x36
	v_add_f32_e32 v224, v224, v225
	v_cmp_gt_i32_e64 s[4:5], 0, v224
	v_not_b32_e32 v225, v224
	v_or_b32_e32 v238, 0x80000000, v224
	v_cndmask_b32_e64 v224, v238, v225, s[4:5]
	v_and_b32_e32 v224, 0xffffff00, v224
	v_bitop3_b32 v87, v224, s19, v87 bitop3:0x36
	v_add_f32_e32 v226, v226, v227
	v_cmp_gt_i32_e64 s[4:5], 0, v226
	v_not_b32_e32 v227, v226
	v_or_b32_e32 v238, 0x80000000, v226
	v_cndmask_b32_e64 v226, v238, v227, s[4:5]
	v_and_b32_e32 v226, 0xffffff00, v226
	v_bitop3_b32 v90, v226, s19, v90 bitop3:0x36
	v_add_f32_e32 v228, v228, v229
	v_cmp_gt_i32_e64 s[4:5], 0, v228
	v_not_b32_e32 v229, v228
	v_or_b32_e32 v238, 0x80000000, v228
	v_cndmask_b32_e64 v228, v238, v229, s[4:5]
	v_and_b32_e32 v228, 0xffffff00, v228
	v_bitop3_b32 v89, v228, s19, v89 bitop3:0x36
	v_add_f32_e32 v230, v230, v231
	v_cmp_gt_i32_e64 s[4:5], 0, v230
	v_not_b32_e32 v231, v230
	v_or_b32_e32 v238, 0x80000000, v230
	v_cndmask_b32_e64 v230, v238, v231, s[4:5]
	v_and_b32_e32 v230, 0xffffff00, v230
	v_bitop3_b32 v92, v230, s19, v92 bitop3:0x36
	v_add_f32_e32 v232, v232, v233
	v_cmp_gt_i32_e64 s[4:5], 0, v232
	v_not_b32_e32 v233, v232
	v_or_b32_e32 v238, 0x80000000, v232
	v_cndmask_b32_e64 v232, v238, v233, s[4:5]
	v_and_b32_e32 v232, 0xffffff00, v232
	v_bitop3_b32 v91, v232, s19, v91 bitop3:0x36
	v_add_f32_e32 v234, v234, v235
	v_cmp_gt_i32_e64 s[4:5], 0, v234
	v_not_b32_e32 v235, v234
	v_or_b32_e32 v238, 0x80000000, v234
	v_cndmask_b32_e64 v234, v238, v235, s[4:5]
	v_and_b32_e32 v234, 0xffffff00, v234
	v_bitop3_b32 v94, v234, s19, v94 bitop3:0x36
	v_add_f32_e32 v236, v236, v237
	v_cmp_gt_i32_e64 s[4:5], 0, v236
	v_not_b32_e32 v237, v236
	v_or_b32_e32 v238, 0x80000000, v236
	v_cndmask_b32_e64 v236, v238, v237, s[4:5]
	v_and_b32_e32 v236, 0xffffff00, v236
	v_bitop3_b32 v93, v236, s19, v70 bitop3:0x36
	s_or_b64 exec, exec, s[6:7]
	s_mov_b64 s[4:5], exec
	s_branch .LBB0_1650
